# BEST + reversed N-panel order in the in-projection (g first, u last) so that P3's inputs are the most recently written
# speedup vs baseline: 1.0028x; 1.0028x over previous
;     __device__ __forceinline__ bool tile(int i, int& pm, int& pn) const {
;         const long L = (long)i * G + c; if (L >= nwg) return false;
;         int wgid = (int)L; { const int q = nwg / NXCD, r = nwg % NXCD, xcd = wgid % NXCD, off = wgid / NXCD; wgid = (xcd < r ? xcd * (q + 1) : r * (q + 1) + (xcd - r) * q) + off; }
;         const int nig = WGM * nN, gid = wgid / nig, fm = gid * WGM, gsz = (nM - fm) < WGM ? (nM - fm) : WGM;
;         pm = fm + ((wgid % nig) % gsz); pn = (wgid % nig) / gsz; return true;
;     }
;     __device__ __forceinline__ bool next(int i, g8::Unit& u) const {
;         int pm, pn; if (i + ioff >= iend || !tile(i + ioff, pm, pn)) return false;
;         u.pm = __builtin_amdgcn_readfirstlane(pm); u.pn = __builtin_amdgcn_readfirstlane(pn); u.flags = 0; u.aux = 0;
;         u.aoff = abase + (unsigned)u.pm * 256u * (unsigned)lda * 2u; u.boff = bbase + (unsigned)u.pn * 256u * (unsigned)ldb * 2u; return true;
;     }
.LBB0_221:
	s_and_b64 s[0:1], s[24:25], exec
	s_cselect_b32 s74, 0, s62
	s_cselect_b32 s75, s62, 2.0
	s_cmp_ge_i32 s74, s75
	v_readfirstlane_b32 s30, v0
	s_cbranch_scc1 .LBB0_224
	s_mul_i32 s0, s74, s33
	s_mul_hi_i32 s1, s74, s33
	s_add_u32 s0, s0, s2
	s_addc_u32 s1, s1, s51
	v_cmp_gt_i64_e32 vcc, s[0:1], v[196:197]
	s_cbranch_vccnz .LBB0_225
	s_ashr_i32 s1, s0, 31
	s_lshr_b32 s1, s1, 29
	s_add_i32 s1, s0, s1
	s_ashr_i32 s3, s1, 3
	s_and_b32 s1, s1, -8
	s_sub_i32 s0, s0, s1
	s_cmp_lt_i32 s0, 0
	s_movk_i32 s1, 0xa1
	s_cselect_b32 s1, s1, 0xa0
	s_mul_i32 s0, s0, s1
	s_add_i32 s0, s0, s3
	s_mul_hi_i32 s1, s0, 0x66666667
	s_lshr_b32 s3, s1, 31
	s_ashr_i32 s1, s1, 6
	s_add_i32 s1, s1, s3
	s_lshl_b32 s3, s1, 3
	s_sub_i32 s4, 64, s3
	s_min_i32 s4, s4, 8
	s_abs_i32 s5, s4
	s_waitcnt vmcnt(0)
	v_cvt_f32_u32_e32 v2, s5
	s_sub_i32 s7, 0, s5
	s_mulk_i32 s1, 0xa0
	s_sub_i32 s0, s0, s1
	v_rcp_iflag_f32_e32 v2, v2
	s_abs_i32 s1, s0
	s_xor_b32 s6, s0, s4
	s_ashr_i32 s6, s6, 31
	v_mul_f32_e32 v2, 0x4f7ffffe, v2
	v_cvt_u32_f32_e32 v2, v2
	s_nop 0
	v_readfirstlane_b32 s8, v2
	s_mul_i32 s7, s7, s8
	s_mul_hi_u32 s7, s8, s7
	s_add_i32 s8, s8, s7
	s_mul_hi_u32 s7, s1, s8
	s_mul_i32 s8, s7, s5
	s_sub_i32 s1, s1, s8
	s_add_i32 s9, s7, 1
	s_sub_i32 s8, s1, s5
	s_cmp_ge_u32 s1, s5
	s_cselect_b32 s7, s9, s7
	s_cselect_b32 s1, s8, s1
	s_add_i32 s8, s7, 1
	s_cmp_ge_u32 s1, s5
	s_cselect_b32 s1, s8, s7
	s_xor_b32 s1, s1, s6
	s_sub_i32 s44, s1, s6
	s_mul_i32 s1, s44, s4
	s_sub_i32 s0, s0, s1
	s_add_i32 s73, s3, s0
	s_lshl_b32 s0, s73, 20
	s_add_i32 s14, s0, 0x1b41e000
	s_sub_i32 s44, 19, s44
	s_lshl_b32 s0, s44, 20
	s_add_i32 s6, s0, 0x161e000
	s_mov_b32 s7, s15
	s_mov_b64 s[0:1], s[14:15]
	s_branch .LBB0_226

;     __device__ __forceinline__ bool tile(int i, int& pm, int& pn) const {
;         const long L = (long)i * G + c; if (L >= nwg) return false;
;         int wgid = (int)L; { const int q = nwg / NXCD, r = nwg % NXCD, xcd = wgid % NXCD, off = wgid / NXCD; wgid = (xcd < r ? xcd * (q + 1) : r * (q + 1) + (xcd - r) * q) + off; }
;         const int nig = WGM * nN, gid = wgid / nig, fm = gid * WGM, gsz = (nM - fm) < WGM ? (nM - fm) : WGM;
;         pm = fm + ((wgid % nig) % gsz); pn = (wgid % nig) / gsz; return true;
;     }
;     ...
;         const bool has_next = S.next(ui + 1, nxt);
;     __device__ __forceinline__ bool next(int i, g8::Unit& u) const {
;         int pm, pn; if (i + ioff >= iend || !tile(i + ioff, pm, pn)) return false;
;         u.pm = __builtin_amdgcn_readfirstlane(pm); u.pn = __builtin_amdgcn_readfirstlane(pn); u.flags = 0; u.aux = 0;
;         u.aoff = abase + (unsigned)u.pm * 256u * (unsigned)lda * 2u; u.boff = bbase + (unsigned)u.pn * 256u * (unsigned)ldb * 2u; return true;
;     }
.LBB0_230:
	s_add_i32 s25, s25, 1
	s_add_i32 s34, s25, s74
	s_cmp_ge_i32 s34, s75
	s_mov_b64 s[42:43], 0
	s_cbranch_scc1 .LBB0_233
	s_mul_hi_i32 s4, s34, s33
	s_mul_i32 s34, s34, s33
	s_add_u32 s34, s34, s2
	s_addc_u32 s35, s4, s51
	v_cmp_gt_i64_e32 vcc, s[34:35], v[196:197]
	s_cbranch_vccnz .LBB0_233
	s_ashr_i32 s3, s34, 31
	s_lshr_b32 s3, s3, 29
	s_add_i32 s3, s34, s3
	s_ashr_i32 s4, s3, 3
	s_and_b32 s3, s3, -8
	s_sub_i32 s3, s34, s3
	s_cmp_lt_i32 s3, 0
	s_movk_i32 s5, 0xa1
	s_cselect_b32 s5, s5, 0xa0
	s_mul_i32 s3, s3, s5
	s_add_i32 s3, s3, s4
	s_mul_hi_i32 s4, s3, 0x66666667
	s_lshr_b32 s5, s4, 31
	s_ashr_i32 s4, s4, 6
	s_add_i32 s4, s4, s5
	s_lshl_b32 s5, s4, 3
	s_sub_i32 s34, 64, s5
	s_min_i32 s34, s34, 8
	s_abs_i32 s35, s34
	v_cvt_f32_u32_e32 v2, s35
	s_sub_i32 s37, 0, s35
	s_mulk_i32 s4, 0xa0
	s_sub_i32 s3, s3, s4
	v_rcp_iflag_f32_e32 v2, v2
	s_abs_i32 s4, s3
	s_xor_b32 s36, s3, s34
	s_ashr_i32 s36, s36, 31
	v_mul_f32_e32 v2, 0x4f7ffffe, v2
	v_cvt_u32_f32_e32 v2, v2
	s_mov_b64 s[42:43], -1
	v_readfirstlane_b32 s38, v2
	s_mul_i32 s37, s37, s38
	s_mul_hi_u32 s37, s38, s37
	s_add_i32 s38, s38, s37
	s_mul_hi_u32 s37, s4, s38
	s_mul_i32 s38, s37, s35
	s_sub_i32 s4, s4, s38
	s_add_i32 s39, s37, 1
	s_sub_i32 s38, s4, s35
	s_cmp_ge_u32 s4, s35
	s_cselect_b32 s37, s39, s37
	s_cselect_b32 s4, s38, s4
	s_add_i32 s38, s37, 1
	s_cmp_ge_u32 s4, s35
	s_cselect_b32 s4, s38, s37
	s_xor_b32 s4, s4, s36
	s_sub_i32 s45, s4, s36
	s_mul_i32 s4, s45, s34
	s_sub_i32 s3, s3, s4
	s_add_i32 s3, s5, s3
	s_lshl_b32 s4, s3, 20
	s_add_i32 s9, s4, 0x1b41e000
	s_sub_i32 s45, 19, s45
	s_lshl_b32 s4, s45, 20
	s_add_i32 s66, s4, 0x161e000
